# gate/up unit end: store drain + barrier + completion signal deferred to the next unit's prologue barrier (which already drains)
# speedup vs baseline: 1.0043x; 1.0043x over previous
; #define LAS __attribute__((address_space(3)))
; __device__ __forceinline__ int tid_opaque() { int t = threadIdx.x; asm volatile("" : "+v"(t)); return t; }
; __device__ __forceinline__ __amdgpu_buffer_rsrc_t mk_rsrc(const void* p) { return __builtin_amdgcn_make_buffer_rsrc((void*)p, 0, 0x7ffffff0, 0x00020000); }
; __device__ __forceinline__ int vwg_id() { const int G = gridDim.x; return (G % 8 == 0) ? (int)((blockIdx.x % 8) * (G / 8) + blockIdx.x / 8) : (int)blockIdx.x; }
; __device__ __forceinline__ void phase_moe_gu(const Ptrs& p, LAS unsigned char* lds) {
;     const int* counts = (const int*)(p.ws + OFF_CTRL); const bf16_t* h2 = (const bf16_t*)(p.ws + OFF_HA); bf16_t* act = (bf16_t*)(p.ws + OFF_ACT);
;     const __amdgpu_buffer_rsrc_t ract = __builtin_amdgcn_make_buffer_rsrc((void*)act, 0, 0x7ffffff0, 0x00020000);
;     MoeUnit mu; const int cv = counts[tid_opaque() & 31];
;     for (int u = vwg_id(); moe_unit(cv, u, 16, mu); u += gridDim.x) {
;         GemmT T; T.init();
;         const int* list = (const int*)(p.ws + OFF_LIST) + (size_t)mu.e * NTOK; const int i0 = mu.mt * 256, n0 = mu.nt * 128;
;         unsigned ao[4];
; #pragma unroll
;         for (int i = 0; i < 4; ++i) { const int r = i0 + T.aR + 64 * i; const int tok = (r < mu.cnt) ? (list[r] >> 2) : 0; ao[i] = (unsigned)((tok * D + T.aC) * 2); }
;         const float* wsel = ((__builtin_amdgcn_readfirstlane(T.b_p) & 1) ? p.w_up : p.w_gate) + (size_t)mu.e * D * D + n0;
;         const unsigned bo = (unsigned)((T.b_k * D + T.b_gucol) * 4);
;         f32x4 acc[8][4]; acc_zero(acc);
;         const int mlim = __builtin_amdgcn_readfirstlane(T.wr) ? 0 : ((mu.cnt - i0 + 15) >> 4);
;         if (mu.light) gemm_kloop_light(acc, lds, T, mk_rsrc(h2), ao[0], ao[1], ao[2], ao[3], mk_rsrc(wsel), bo, D * 4u, D / 64, mlim);
;         else gemm_kloop(acc, lds, T, mk_rsrc(h2), ao[0], ao[1], ao[2], ao[3], mk_rsrc(wsel), bo, D * 4u, D / 64);
.LBB0_1003:
	s_add_u32 s20, s30, 0x18248000
	s_addc_u32 s28, s31, 0
	s_and_b32 s21, s28, 0xffff
	s_mov_b32 s27, 0x20000
	s_mov_b32 s26, 0x7ffffff0
	s_and_b32 s37, s37, 0xffff
	s_movk_i32 s66, 0x6000
	s_mov_b32 s67, 0x80000
	s_mov_b32 s76, 0x82000
	s_mov_b32 s77, 0x84000
	s_mov_b32 s78, 0x86000
	s_mov_b32 s79, 0x88000
	s_mov_b32 s80, 0x8a000
	s_mov_b32 s81, 0x8c000
	s_mov_b32 s82, 0x8e000
	s_movk_i32 s83, 0xf80
	s_add_i32 s29, 0, 0x18000
	s_add_i32 s64, 0, 0x10400
	s_mov_b32 s84, 0xc0e00000
	v_mov_b32_e32 v2, 0
	v_mov_b32_e32 v214, 0x40e00000
	s_mov_b32 s98, 0
	s_branch .LBB0_1006

; #define G_DMA_A(buf, t, i_) __builtin_amdgcn_raw_ptr_buffer_load_lds(ra, (LAS void*)(lds + (buf) * 65536 + a_wu + (i_) * 8192), 16, ao##i_, (unsigned)(t) * 128u, 0, 0)
; #define G_ISSUE_B(t) do { const unsigned so_ = (unsigned)(t) * 64u * ldbB; _Pragma("unroll") for (int i_ = 0; i_ < 8; ++i_) sb[i_] = __builtin_bit_cast(f32x4, __builtin_amdgcn_raw_buffer_load_b128(rb, bo, so_ + (unsigned)i_ * ldbB, 0)); } while (0)
; #define G_RETIRE() asm volatile("s_waitcnt vmcnt(0)" : "+v"(sb[0]), "+v"(sb[1]), "+v"(sb[2]), "+v"(sb[3]), "+v"(sb[4]), "+v"(sb[5]), "+v"(sb[6]), "+v"(sb[7]) :: "memory")
; #define G_WRITE_B(buf) do { LAS unsigned char* d_ = lds + (buf) * 65536; \
;         _Pragma("unroll") for (int j_ = 0; j_ < 4; ++j_) { u32x4 w_; w_.x = cvtpk(sb[0][j_], sb[1][j_]); w_.y = cvtpk(sb[2][j_], sb[3][j_]); w_.z = cvtpk(sb[4][j_], sb[5][j_]); w_.w = cvtpk(sb[6][j_], sb[7][j_]); \
;             *(LAS u32x4*)(d_ + 32768 + T.b_w + ((T.b_rot + 64u * j_) & 255u)) = w_; } } while (0)
; #define G_BAR() do { asm volatile("s_waitcnt lgkmcnt(0)" ::: "memory"); __builtin_amdgcn_s_barrier(); asm volatile("" ::: "memory"); } while (0)
; #define G_DMA_A(buf, t, i_) __builtin_amdgcn_raw_ptr_buffer_load_lds(ra, (LAS void*)(lds + (buf) * 65536 + a_wu + (i_) * 8192), 16, ao##i_, (unsigned)(t) * 128u, 0, 0)
; #define G_ISSUE_B(t) do { const unsigned so_ = (unsigned)(t) * 64u * ldbB; _Pragma("unroll") for (int i_ = 0; i_ < 8; ++i_) sb[i_] = __builtin_bit_cast(f32x4, __builtin_amdgcn_raw_buffer_load_b128(rb, bo, so_ + (unsigned)i_ * ldbB, 0)); } while (0)
; #define G_RETIRE() asm volatile("s_waitcnt vmcnt(0)" : "+v"(sb[0]), "+v"(sb[1]), "+v"(sb[2]), "+v"(sb[3]), "+v"(sb[4]), "+v"(sb[5]), "+v"(sb[6]), "+v"(sb[7]) :: "memory")
; __device__ __forceinline__ void gemm_kloop_light(f32x4 (&acc)[8][4], LAS unsigned char* lds, const GemmT& T, ...
;     ...
;     G_ISSUE_B(0); G_DMA_A(0, 0, 0); G_DMA_A(0, 0, 1); G_DMA_A(0, 0, 2); G_DMA_A(0, 0, 3); G_RETIRE(); G_WRITE_B(0);
;     if (nt > 1) G_ISSUE_B(1);
;     G_BAR();
; __device__ __forceinline__ void phase_moe_gu(const Ptrs& p, LAS unsigned char* lds) {
;     ...
;         if (threadIdx.x == 0) { __hip_atomic_fetch_add((unsigned*)(p.ws + OFF_GUDONE) + mu.e * 16, 1u, __ATOMIC_RELAXED, __HIP_MEMORY_SCOPE_AGENT);
;                                 __hip_atomic_fetch_add((unsigned*)(p.ws + OFF_GUTOT), 1u, __ATOMIC_RELAXED, __HIP_MEMORY_SCOPE_AGENT); }
.Lmy_rcgP1:
	buffer_load_dwordx4 v[162:165], v225, s[24:27], s67 offen
	buffer_load_dwordx4 v[166:169], v225, s[24:27], s76 offen
	buffer_load_dwordx4 v[170:173], v225, s[24:27], s77 offen
	buffer_load_dwordx4 v[174:177], v225, s[24:27], s78 offen
	buffer_load_dwordx4 v[178:181], v225, s[24:27], s79 offen
	buffer_load_dwordx4 v[182:185], v225, s[24:27], s80 offen
	buffer_load_dwordx4 v[186:189], v225, s[24:27], s81 offen
	buffer_load_dwordx4 v[190:193], v225, s[24:27], s82 offen
	s_cmp_gt_i32 s1, 0
	s_cselect_b64 s[62:63], -1, 0
	s_cmp_lg_u32 s1, 1
	v_cvt_pk_bf16_f32 v36, v12, v32
	v_cvt_pk_bf16_f32 v37, v20, v4
	v_cvt_pk_bf16_f32 v38, v24, v8
	v_cvt_pk_bf16_f32 v39, v28, v16
	s_cselect_b64 s[60:61], -1, 0
	s_cmp_gt_i32 s1, 2
	ds_write_b128 v228, v[36:39] offset:32768
	v_cvt_pk_bf16_f32 v36, v13, v33
	v_cvt_pk_bf16_f32 v37, v21, v5
	v_cvt_pk_bf16_f32 v38, v25, v9
	v_cvt_pk_bf16_f32 v39, v29, v17
	s_cselect_b64 s[58:59], -1, 0
	s_cmp_gt_i32 s1, 3
	ds_write_b128 v228, v[36:39] offset:32832
	v_cvt_pk_bf16_f32 v36, v14, v34
	v_cvt_pk_bf16_f32 v37, v22, v6
	v_cvt_pk_bf16_f32 v38, v26, v10
	v_cvt_pk_bf16_f32 v39, v30, v18
	v_cvt_pk_bf16_f32 v4, v15, v35
	v_cvt_pk_bf16_f32 v5, v23, v7
	v_cvt_pk_bf16_f32 v6, v27, v11
	v_cvt_pk_bf16_f32 v7, v31, v19
	v_add_u32_e32 v3, v227, v218
	s_cselect_b64 s[54:55], -1, 0
	s_cmp_gt_i32 s1, 4
	ds_write_b128 v228, v[36:39] offset:32896
	ds_write_b128 v3, v[4:7] offset:32768
	s_cselect_b64 s[46:47], -1, 0
	s_cmp_gt_i32 s1, 5
	s_waitcnt lgkmcnt(0)
	s_barrier
	s_cselect_b64 s[44:45], -1, 0
	s_cmp_eq_u32 s98, 0
	s_cbranch_scc1 .Lmy_sig_skipL
	v_readlane_b32 vcc_lo, v246, 8
	v_readlane_b32 vcc_hi, v246, 9
	s_nop 3
	s_and_saveexec_b64 s[6:7], vcc
	s_cbranch_execz .Lmy_sig_resL
	s_add_i32 vcc_lo, s98, -1
	s_lshl_b32 vcc_lo, vcc_lo, 6
	v_mov_b32_e32 v244, 1
	v_mov_b32_e32 v245, vcc_lo
	global_atomic_add v245, v244, s[30:31] offset:2048
	global_atomic_add v2, v244, s[30:31] offset:1024
.Lmy_sig_resL:
	s_mov_b64 exec, s[6:7]
	s_mov_b32 s98, 0
.Lmy_sig_skipL:
	s_cmp_gt_i32 s1, 6
	v_mov_b32_e32 v4, v2
	v_mov_b32_e32 v5, v2
	s_cselect_b64 s[34:35], -1, 0
	s_cmp_gt_i32 s1, 7
	v_mov_b32_e32 v3, v2
	v_mov_b64_e32 v[16:17], v[4:5]
	v_mov_b64_e32 v[8:9], v[4:5]
	v_mov_b64_e32 v[20:21], v[4:5]
	v_mov_b64_e32 v[12:13], v[4:5]
	v_mov_b64_e32 v[32:33], v[4:5]
	v_mov_b64_e32 v[24:25], v[4:5]
	v_mov_b64_e32 v[36:37], v[4:5]
	v_mov_b64_e32 v[28:29], v[4:5]
	v_mov_b64_e32 v[48:49], v[4:5]
	v_mov_b64_e32 v[40:41], v[4:5]
	v_mov_b64_e32 v[52:53], v[4:5]
	v_mov_b64_e32 v[44:45], v[4:5]
	v_mov_b64_e32 v[64:65], v[4:5]
	v_mov_b64_e32 v[56:57], v[4:5]
	v_mov_b64_e32 v[68:69], v[4:5]
	v_mov_b64_e32 v[60:61], v[4:5]
	v_mov_b64_e32 v[80:81], v[4:5]
	v_mov_b64_e32 v[72:73], v[4:5]
	v_mov_b64_e32 v[84:85], v[4:5]
	v_mov_b64_e32 v[76:77], v[4:5]
	v_mov_b64_e32 v[96:97], v[4:5]
	v_mov_b64_e32 v[88:89], v[4:5]
	v_mov_b64_e32 v[100:101], v[4:5]
	v_mov_b64_e32 v[92:93], v[4:5]
	v_mov_b64_e32 v[112:113], v[4:5]
	v_mov_b64_e32 v[104:105], v[4:5]
	v_mov_b64_e32 v[140:141], v[4:5]
	v_mov_b64_e32 v[108:109], v[4:5]
	v_mov_b64_e32 v[160:161], v[4:5]
	v_mov_b64_e32 v[152:153], v[4:5]
	v_mov_b64_e32 v[196:197], v[4:5]
	v_mov_b64_e32 v[156:157], v[4:5]
	s_mov_b32 s68, 0
	s_cselect_b64 s[22:23], -1, 0
	s_mov_b32 s69, 0x10e000
	s_movk_i32 s70, 0x80
	v_mov_b64_e32 v[14:15], v[2:3]
	v_mov_b64_e32 v[6:7], v[2:3]
	v_mov_b64_e32 v[18:19], v[2:3]
	v_mov_b64_e32 v[10:11], v[2:3]
	v_mov_b64_e32 v[30:31], v[2:3]
	v_mov_b64_e32 v[22:23], v[2:3]
	v_mov_b64_e32 v[34:35], v[2:3]
	v_mov_b64_e32 v[26:27], v[2:3]
	v_mov_b64_e32 v[46:47], v[2:3]
	v_mov_b64_e32 v[38:39], v[2:3]
	v_mov_b64_e32 v[50:51], v[2:3]
	v_mov_b64_e32 v[42:43], v[2:3]
	v_mov_b64_e32 v[62:63], v[2:3]
	v_mov_b64_e32 v[54:55], v[2:3]
	v_mov_b64_e32 v[66:67], v[2:3]
	v_mov_b64_e32 v[58:59], v[2:3]
	v_mov_b64_e32 v[78:79], v[2:3]
	v_mov_b64_e32 v[70:71], v[2:3]
	v_mov_b64_e32 v[82:83], v[2:3]
	v_mov_b64_e32 v[74:75], v[2:3]
	v_mov_b64_e32 v[94:95], v[2:3]
	v_mov_b64_e32 v[86:87], v[2:3]
	v_mov_b64_e32 v[98:99], v[2:3]
	v_mov_b64_e32 v[90:91], v[2:3]
	v_mov_b64_e32 v[110:111], v[2:3]
	v_mov_b64_e32 v[102:103], v[2:3]
	v_mov_b64_e32 v[138:139], v[2:3]
	v_mov_b64_e32 v[106:107], v[2:3]
	v_mov_b64_e32 v[158:159], v[2:3]
	v_mov_b64_e32 v[150:151], v[2:3]
	v_mov_b64_e32 v[194:195], v[2:3]
	v_mov_b64_e32 v[154:155], v[2:3]
	s_cmp_ge_i32 s100, 32
	s_cbranch_scc0 .Lmy_d2g_nopre
	s_mov_b32 s98, 0x10e000
	s_add_i32 s6, s98, 0xffff2000
	buffer_load_dwordx4 v[8:11], v225, s[24:27], s6 offen
	s_add_i32 s7, s98, 0xffff4000
	buffer_load_dwordx4 v[12:15], v225, s[24:27], s7 offen
	s_add_i32 s6, s98, 0xffff6000
	buffer_load_dwordx4 v[16:19], v225, s[24:27], s6 offen
	s_add_i32 s7, s98, 0xffff8000
	buffer_load_dwordx4 v[20:23], v225, s[24:27], s7 offen
	s_add_i32 s6, s98, 0xffffa000
	buffer_load_dwordx4 v[24:27], v225, s[24:27], s6 offen
	s_add_i32 s7, s98, 0xffffc000
	buffer_load_dwordx4 v[28:31], v225, s[24:27], s7 offen
	s_add_i32 s6, s98, 0xffffe000
	buffer_load_dwordx4 v[32:35], v225, s[24:27], s6 offen
	buffer_load_dwordx4 v[36:39], v225, s[24:27], s98 offen

; #define G_DMA_A(buf, t, i_) __builtin_amdgcn_raw_ptr_buffer_load_lds(ra, (LAS void*)(lds + (buf) * 65536 + a_wu + (i_) * 8192), 16, ao##i_, (unsigned)(t) * 128u, 0, 0)
; #define G_ISSUE_B(t) do { const unsigned so_ = (unsigned)(t) * 64u * ldbB; _Pragma("unroll") for (int i_ = 0; i_ < 8; ++i_) sb[i_] = __builtin_bit_cast(f32x4, __builtin_amdgcn_raw_buffer_load_b128(rb, bo, so_ + (unsigned)i_ * ldbB, 0)); } while (0)
; #define G_RETIRE() asm volatile("s_waitcnt vmcnt(0)" : "+v"(sb[0]), "+v"(sb[1]), "+v"(sb[2]), "+v"(sb[3]), "+v"(sb[4]), "+v"(sb[5]), "+v"(sb[6]), "+v"(sb[7]) :: "memory")
; #define G_WRITE_B(buf) do { LAS unsigned char* d_ = lds + (buf) * 65536; \
;         _Pragma("unroll") for (int j_ = 0; j_ < 4; ++j_) { u32x4 w_; w_.x = cvtpk(sb[0][j_], sb[1][j_]); w_.y = cvtpk(sb[2][j_], sb[3][j_]); w_.z = cvtpk(sb[4][j_], sb[5][j_]); w_.w = cvtpk(sb[6][j_], sb[7][j_]); \
;             *(LAS u32x4*)(d_ + 32768 + T.b_w + ((T.b_rot + 64u * j_) & 255u)) = w_; } } while (0)
; #define G_BAR() do { asm volatile("s_waitcnt lgkmcnt(0)" ::: "memory"); __builtin_amdgcn_s_barrier(); asm volatile("" ::: "memory"); } while (0)
; #define G_DMA_A(buf, t, i_) __builtin_amdgcn_raw_ptr_buffer_load_lds(ra, (LAS void*)(lds + (buf) * 65536 + a_wu + (i_) * 8192), 16, ao##i_, (unsigned)(t) * 128u, 0, 0)
; #define G_ISSUE_B(t) do { const unsigned so_ = (unsigned)(t) * 64u * ldbB; _Pragma("unroll") for (int i_ = 0; i_ < 8; ++i_) sb[i_] = __builtin_bit_cast(f32x4, __builtin_amdgcn_raw_buffer_load_b128(rb, bo, so_ + (unsigned)i_ * ldbB, 0)); } while (0)
; __device__ __forceinline__ void gemm_kloop(f32x4 (&acc)[8][4], LAS unsigned char* lds, const GemmT& T, ...
;     ...
;     bf16x8 Bf0[4], Bf1[4], AtA[4], AtB[4];
;     G_ISSUE_B(0); G_DMA_A(0, 0, 0); G_DMA_A(0, 0, 1); G_DMA_A(0, 0, 2); G_DMA_A(0, 0, 3); G_RETIRE(); G_WRITE_B(0);
;     if (nt > 1) G_ISSUE_B(1);
;     G_BAR();
; __device__ __forceinline__ void phase_moe_gu(const Ptrs& p, LAS unsigned char* lds) {
;     ...
;         if (threadIdx.x == 0) { __hip_atomic_fetch_add((unsigned*)(p.ws + OFF_GUDONE) + mu.e * 16, 1u, __ATOMIC_RELAXED, __HIP_MEMORY_SCOPE_AGENT);
;                                 __hip_atomic_fetch_add((unsigned*)(p.ws + OFF_GUTOT), 1u, __ATOMIC_RELAXED, __HIP_MEMORY_SCOPE_AGENT); }
.LBB0_1263:
	s_cbranch_execz .LBB0_1267
	v_readfirstlane_b32 s1, v229
	s_and_b32 s1, s1, 0xfffffc00
	s_add_i32 s1, s1, 0
	s_mov_b32 s38, s26
	s_mov_b32 s39, s27
	s_mov_b32 m0, s1
	v_add_u32_e32 v3, v227, v218
	buffer_load_dwordx4 v223, s[36:39], 0 offen lds
	s_add_i32 m0, s1, 0x2000
	v_mov_b32_e32 v36, 0
	buffer_load_dwordx4 v222, s[36:39], 0 offen lds
	s_add_i32 m0, s1, 0x4000
	s_mov_b32 s3, 0
	buffer_load_dwordx4 v221, s[36:39], 0 offen lds
	s_add_i32 m0, s1, 0x6000
	s_mov_b32 s4, 0x10e000
	buffer_load_dwordx4 v224, s[36:39], 0 offen lds
	s_waitcnt vmcnt(4)
	s_waitcnt vmcnt(0)
	s_movk_i32 s5, 0x80
	v_cvt_pk_bf16_f32 v4, v114, v126
	v_cvt_pk_bf16_f32 v5, v130, v118
	v_cvt_pk_bf16_f32 v6, v122, v134
	v_cvt_pk_bf16_f32 v7, v142, v146
	ds_write_b128 v228, v[4:7] offset:32768
	v_cvt_pk_bf16_f32 v4, v115, v127
	v_cvt_pk_bf16_f32 v5, v131, v119
	v_cvt_pk_bf16_f32 v6, v123, v135
	v_cvt_pk_bf16_f32 v7, v143, v147
	ds_write_b128 v228, v[4:7] offset:32832
	v_cvt_pk_bf16_f32 v4, v116, v128
	v_cvt_pk_bf16_f32 v5, v132, v120
	v_cvt_pk_bf16_f32 v6, v124, v136
	v_cvt_pk_bf16_f32 v7, v144, v148
	ds_write_b128 v228, v[4:7] offset:32896
	v_cvt_pk_bf16_f32 v4, v117, v129
	v_cvt_pk_bf16_f32 v5, v133, v121
	v_cvt_pk_bf16_f32 v6, v125, v137
	v_cvt_pk_bf16_f32 v7, v145, v149
	ds_write_b128 v3, v[4:7] offset:32768
	buffer_load_dwordx4 v[4:7], v225, s[24:27], s67 offen
	buffer_load_dwordx4 v[8:11], v225, s[24:27], s76 offen
	buffer_load_dwordx4 v[12:15], v225, s[24:27], s77 offen
	buffer_load_dwordx4 v[16:19], v225, s[24:27], s78 offen
	buffer_load_dwordx4 v[20:23], v225, s[24:27], s79 offen
	buffer_load_dwordx4 v[28:31], v225, s[24:27], s80 offen
	buffer_load_dwordx4 v[24:27], v225, s[24:27], s81 offen
	buffer_load_dwordx4 v[32:35], v225, s[24:27], s82 offen
	s_waitcnt lgkmcnt(0)
	s_barrier
	s_cmp_eq_u32 s98, 0
	s_cbranch_scc1 .Lmy_sig_skipF
	v_readlane_b32 vcc_lo, v246, 8
	v_readlane_b32 vcc_hi, v246, 9
	s_nop 3
	s_and_saveexec_b64 s[6:7], vcc
	s_cbranch_execz .Lmy_sig_resF
	s_add_i32 vcc_lo, s98, -1
	s_lshl_b32 vcc_lo, vcc_lo, 6
	v_mov_b32_e32 v244, 1
	v_mov_b32_e32 v245, vcc_lo
	global_atomic_add v245, v244, s[30:31] offset:2048
	global_atomic_add v2, v244, s[30:31] offset:1024

; __device__ __forceinline__ void acc_zero(f32x4 (&acc)[8][4]) {
; #pragma unroll
;     for (int m = 0; m < 8; ++m)
; #pragma unroll
;         for (int n = 0; n < 4; ++n) acc[m][n] = (f32x4){0.f, 0.f, 0.f, 0.f};
.Lmy_sig_skipF:
	v_mov_b32_e32 v37, v36
	v_mov_b32_e32 v38, v36
	v_mov_b32_e32 v39, v36
	v_mov_b32_e32 v40, v36
	v_mov_b32_e32 v41, v36
	v_mov_b32_e32 v42, v36
	v_mov_b32_e32 v43, v36
	v_mov_b32_e32 v44, v36
	v_mov_b32_e32 v45, v36
	v_mov_b32_e32 v46, v36
	v_mov_b32_e32 v47, v36
	v_mov_b32_e32 v48, v36
	v_mov_b32_e32 v49, v36
	v_mov_b32_e32 v50, v36
	v_mov_b32_e32 v51, v36
	v_mov_b32_e32 v52, v36
	v_mov_b32_e32 v53, v36
	v_mov_b32_e32 v54, v36
	v_mov_b32_e32 v55, v36
	v_mov_b32_e32 v56, v36
	v_mov_b32_e32 v57, v36
	v_mov_b32_e32 v58, v36
	v_mov_b32_e32 v59, v36
	v_mov_b32_e32 v60, v36
	v_mov_b32_e32 v61, v36
	v_mov_b32_e32 v62, v36
	v_mov_b32_e32 v63, v36
	v_mov_b32_e32 v64, v36
	v_mov_b32_e32 v65, v36
	v_mov_b32_e32 v66, v36
	v_mov_b32_e32 v67, v36
	v_mov_b32_e32 v68, v36
	v_mov_b32_e32 v69, v36
	v_mov_b32_e32 v70, v36
	v_mov_b32_e32 v71, v36
	v_mov_b32_e32 v72, v36
	v_mov_b32_e32 v73, v36
	v_mov_b32_e32 v74, v36
	v_mov_b32_e32 v75, v36
	v_mov_b32_e32 v76, v36
	v_mov_b32_e32 v77, v36
	v_mov_b32_e32 v78, v36
	v_mov_b32_e32 v79, v36
	v_mov_b32_e32 v80, v36
	v_mov_b32_e32 v81, v36
	v_mov_b32_e32 v82, v36
	v_mov_b32_e32 v83, v36
	v_mov_b32_e32 v84, v36
	v_mov_b32_e32 v85, v36
	v_mov_b32_e32 v86, v36
	v_mov_b32_e32 v87, v36
	v_mov_b32_e32 v88, v36
	v_mov_b32_e32 v89, v36
	v_mov_b32_e32 v90, v36
	v_mov_b32_e32 v91, v36
	v_mov_b32_e32 v92, v36
	v_mov_b32_e32 v93, v36
	v_mov_b32_e32 v94, v36
	v_mov_b32_e32 v95, v36
	v_mov_b32_e32 v96, v36
	v_mov_b32_e32 v97, v36
	v_mov_b32_e32 v98, v36
	v_mov_b32_e32 v99, v36
	v_mov_b32_e32 v100, v36
	v_mov_b32_e32 v101, v36
	v_mov_b32_e32 v102, v36
	v_mov_b32_e32 v103, v36
	v_mov_b32_e32 v104, v36
	v_mov_b32_e32 v105, v36
	v_mov_b32_e32 v106, v36
	v_mov_b32_e32 v107, v36
	v_mov_b32_e32 v108, v36
	v_mov_b32_e32 v109, v36
	v_mov_b32_e32 v110, v36
	v_mov_b32_e32 v111, v36
	v_mov_b32_e32 v112, v36
	v_mov_b32_e32 v113, v36
	v_mov_b32_e32 v114, v36
	v_mov_b32_e32 v115, v36
	v_mov_b32_e32 v116, v36
	v_mov_b32_e32 v117, v36
	v_mov_b32_e32 v118, v36
	v_mov_b32_e32 v119, v36
	v_mov_b32_e32 v120, v36
	v_mov_b32_e32 v121, v36
	v_mov_b32_e32 v122, v36
	v_mov_b32_e32 v123, v36
	v_mov_b32_e32 v124, v36
	v_mov_b32_e32 v125, v36
	v_mov_b32_e32 v126, v36
	v_mov_b32_e32 v127, v36
	v_mov_b32_e32 v128, v36
	v_mov_b32_e32 v129, v36
	v_mov_b32_e32 v130, v36
	v_mov_b32_e32 v131, v36
	v_mov_b32_e32 v132, v36
	v_mov_b32_e32 v133, v36
	v_mov_b32_e32 v134, v36
	v_mov_b32_e32 v135, v36
	v_mov_b32_e32 v136, v36
	v_mov_b32_e32 v137, v36
	v_mov_b32_e32 v138, v36
	v_mov_b32_e32 v139, v36
	v_mov_b32_e32 v140, v36
	v_mov_b32_e32 v141, v36
	v_mov_b32_e32 v142, v36
	v_mov_b32_e32 v143, v36
	v_mov_b32_e32 v144, v36
	v_mov_b32_e32 v145, v36
	v_mov_b32_e32 v146, v36
	v_mov_b32_e32 v147, v36
	v_mov_b32_e32 v148, v36
	v_mov_b32_e32 v149, v36
	v_mov_b32_e32 v150, v36
	v_mov_b32_e32 v151, v36
	v_mov_b32_e32 v152, v36
	v_mov_b32_e32 v153, v36
	v_mov_b32_e32 v154, v36
	v_mov_b32_e32 v155, v36
	v_mov_b32_e32 v156, v36
	v_mov_b32_e32 v157, v36
	v_mov_b32_e32 v158, v36
	v_mov_b32_e32 v159, v36
	v_mov_b32_e32 v160, v36
	v_mov_b32_e32 v161, v36
	v_mov_b32_e32 v162, v36
	v_mov_b32_e32 v163, v36

; __device__ __forceinline__ u32x4 pack8(const f32x4 a, const f32x4 b) { u32x4 w; w.x = cvtpk(a[0], a[1]); w.y = cvtpk(a[2], a[3]); w.z = cvtpk(b[0], b[1]); w.w = cvtpk(b[2], b[3]); return w; }
; __device__ __forceinline__ void phase_moe_gu(const Ptrs& p, LAS unsigned char* lds) {
;     ...
;             if (r < mu.cnt) __builtin_amdgcn_raw_buffer_store_b128(pack8(g0, g1), ract, (unsigned)(((mu.base + r) * D + c) * 2), 0, 16); }
;         asm volatile("s_waitcnt vmcnt(0)" ::: "memory");
;         __syncthreads();
;         if (threadIdx.x == 0) { __hip_atomic_fetch_add((unsigned*)(p.ws + OFF_GUDONE) + mu.e * 16, 1u, __ATOMIC_RELAXED, __HIP_MEMORY_SCOPE_AGENT);
;                                 __hip_atomic_fetch_add((unsigned*)(p.ws + OFF_GUTOT), 1u, __ATOMIC_RELAXED, __HIP_MEMORY_SCOPE_AGENT); }
;     }
.LBB0_1283:
	s_or_b64 exec, exec, s[0:1]
	s_add_i32 s98, s42, 1
	s_mov_b64 s[0:1], exec
	s_branch .LBB0_1004
.LBB0_1288:
	s_waitcnt vmcnt(0)
	s_barrier
	s_cmp_eq_u32 s98, 0
	s_cbranch_scc1 .Lmy_sig_skipE
	v_readlane_b32 vcc_lo, v246, 8
	v_readlane_b32 vcc_hi, v246, 9
	s_nop 3
	s_and_saveexec_b64 s[6:7], vcc
	s_cbranch_execz .Lmy_sig_resE
	s_add_i32 vcc_lo, s98, -1
	s_lshl_b32 vcc_lo, vcc_lo, 6
	v_mov_b32_e32 v244, 1
	v_mov_b32_e32 v245, vcc_lo
	global_atomic_add v245, v244, s[30:31] offset:2048
	global_atomic_add v2, v244, s[30:31] offset:1024
